# P8 slot assignment aggregated per workgroup: LDS rank atomics + one returning global atomic per expert per workgroup (32 instead of 256), slot = base + rank
# speedup vs baseline: 1.0295x; 1.0294x over previous
.LBB0_1275:
	s_mulk_i32 s18, 0x840
	s_add_i32 s12, s18, 0
	s_cmpk_lt_u32 s3, 0x100
	s_cselect_b64 s[4:5], -1, 0
	s_cmpk_gt_u32 s3, 0xff
	v_mbcnt_lo_u32_b32 v77, -1, 0
	v_mbcnt_hi_u32_b32 v77, -1, v77
	v_lshlrev_b32_e32 v78, 2, v77
	v_add_u32_e32 v78, 0x21040, v78
	v_mov_b32_e32 v79, 0
	ds_write_b32 v78, v79
	s_waitcnt lgkmcnt(0)
	s_barrier
	s_cbranch_scc1 .LBB0_1277
	ds_read_b128 v[12:15], v10 offset:16896
	ds_read_b128 v[16:19], v10 offset:16912
	v_mul_u32_u24_e32 v10, 0x210, v32
	v_lshlrev_b32_e32 v1, 2, v1
	v_add3_u32 v1, s12, v10, v1
	s_waitcnt lgkmcnt(1)
	v_add_f32_e32 v2, v2, v12
	s_waitcnt lgkmcnt(0)
	v_add_f32_e32 v6, v6, v16
	ds_write2_b32 v1, v2, v6 offset1:16
	v_add_f32_e32 v2, v3, v13
	v_add_f32_e32 v3, v7, v17
	ds_write2_b32 v1, v2, v3 offset0:33 offset1:49
	v_add_f32_e32 v2, v4, v14
	v_add_f32_e32 v3, v8, v18
	ds_write2_b32 v1, v2, v3 offset0:66 offset1:82
	v_add_f32_e32 v2, v5, v15
	v_add_f32_e32 v3, v9, v19
	ds_write2_b32 v1, v2, v3 offset0:99 offset1:115
.LBB0_1277:
	s_waitcnt lgkmcnt(0)
	v_cmp_gt_u32_e32 vcc, 16, v33
	s_and_b64 s[8:9], vcc, s[8:9]
	s_and_b64 s[8:9], s[4:5], s[8:9]
	s_mov_b64 s[96:97], 0
	s_and_saveexec_b64 s[4:5], s[8:9]
	s_cbranch_execz .LBB0_1279
	s_mov_b64 s[96:97], exec
	v_mov_b32_e32 v72, 0x21040
	v_mov_b32_e32 v73, 1
	v_mov_b32_e32 v5, 0
	global_load_dwordx4 v[6:9], v5, s[10:11]
	global_load_dwordx4 v[10:13], v5, s[10:11] offset:16
	global_load_dwordx4 v[16:19], v5, s[10:11] offset:32
	global_load_dwordx4 v[20:23], v5, s[10:11] offset:48
	global_load_dwordx4 v[24:27], v5, s[10:11] offset:64
	global_load_dwordx4 v[28:31], v5, s[10:11] offset:80
	global_load_dwordx4 v[34:37], v5, s[10:11] offset:96
	global_load_dwordx4 v[38:41], v5, s[10:11] offset:112
	v_or_b32_e32 v14, s2, v33
	s_movk_i32 s2, 0x84
	v_mov_b32_e32 v1, s12
	v_mad_u32_u24 v1, v33, s2, v1
	ds_read2_b32 v[2:3], v1 offset1:1
	ds_read2_b32 v[32:33], v1 offset0:2 offset1:3
	ds_read2_b32 v[42:43], v1 offset0:4 offset1:5
	ds_read2_b32 v[44:45], v1 offset0:6 offset1:7
	ds_read2_b32 v[46:47], v1 offset0:8 offset1:9
	ds_read2_b32 v[48:49], v1 offset0:10 offset1:11
	ds_read2_b32 v[50:51], v1 offset0:12 offset1:13
	ds_read2_b32 v[52:53], v1 offset0:14 offset1:15
	ds_read2_b32 v[54:55], v1 offset0:16 offset1:17
	ds_read2_b32 v[56:57], v1 offset0:18 offset1:19
	ds_read2_b32 v[58:59], v1 offset0:20 offset1:21
	ds_read2_b32 v[60:61], v1 offset0:22 offset1:23
	ds_read2_b32 v[62:63], v1 offset0:24 offset1:25
	ds_read2_b32 v[64:65], v1 offset0:26 offset1:27
	ds_read2_b32 v[66:67], v1 offset0:28 offset1:29
	ds_read2_b32 v[68:69], v1 offset0:30 offset1:31
	s_add_u32 s10, s6, 0x4600
	s_addc_u32 s11, s7, 0
	s_add_u32 s8, s6, 0x5f30000
	s_addc_u32 s9, s7, 0
	s_waitcnt vmcnt(7) lgkmcnt(14)
	v_add_f32_e32 v1, v2, v6
	v_add_f32_e32 v4, v3, v7
	v_max_f32_e32 v2, 0xff800000, v1
	v_cmp_gt_f32_e32 vcc, v4, v2
	v_add_f32_e32 v6, v32, v8
	v_add_f32_e32 v7, v33, v9
	v_cndmask_b32_e32 v2, v2, v4, vcc
	v_cndmask_b32_e64 v3, 0, 1, vcc
	v_cmp_gt_f32_e32 vcc, v6, v2
	s_waitcnt vmcnt(6) lgkmcnt(13)
	v_add_f32_e32 v8, v42, v10
	v_add_f32_e32 v9, v43, v11
	v_cndmask_b32_e32 v2, v2, v6, vcc
	v_cndmask_b32_e64 v3, v3, 2, vcc
	v_cmp_gt_f32_e32 vcc, v7, v2
	s_waitcnt lgkmcnt(12)
	v_add_f32_e32 v10, v44, v12
	v_add_f32_e32 v11, v45, v13
	v_cndmask_b32_e32 v2, v2, v7, vcc
	v_cndmask_b32_e64 v3, v3, 3, vcc
	v_cmp_gt_f32_e32 vcc, v8, v2
	s_waitcnt vmcnt(5) lgkmcnt(11)
	v_add_f32_e32 v12, v46, v16
	v_add_f32_e32 v13, v47, v17
	v_cndmask_b32_e32 v2, v2, v8, vcc
	v_cndmask_b32_e64 v3, v3, 4, vcc
	v_cmp_gt_f32_e32 vcc, v9, v2
	s_waitcnt lgkmcnt(10)
	v_add_f32_e32 v15, v48, v18
	v_add_f32_e32 v16, v49, v19
	v_cndmask_b32_e32 v2, v2, v9, vcc
	v_cndmask_b32_e64 v3, v3, 5, vcc
	v_cmp_gt_f32_e32 vcc, v10, v2
	s_waitcnt vmcnt(4) lgkmcnt(9)
	v_add_f32_e32 v17, v50, v20
	v_add_f32_e32 v18, v51, v21
	v_cndmask_b32_e32 v2, v2, v10, vcc
	v_cndmask_b32_e64 v3, v3, 6, vcc
	v_cmp_gt_f32_e32 vcc, v11, v2
	s_waitcnt lgkmcnt(8)
	v_add_f32_e32 v19, v52, v22
	v_add_f32_e32 v20, v53, v23
	v_cndmask_b32_e32 v2, v2, v11, vcc
	v_cndmask_b32_e64 v3, v3, 7, vcc
	v_cmp_gt_f32_e32 vcc, v12, v2
	s_waitcnt vmcnt(3) lgkmcnt(7)
	v_add_f32_e32 v21, v54, v24
	v_add_f32_e32 v22, v55, v25
	v_cndmask_b32_e32 v2, v2, v12, vcc
	v_cndmask_b32_e64 v3, v3, 8, vcc
	v_cmp_gt_f32_e32 vcc, v13, v2
	s_waitcnt lgkmcnt(6)
	v_add_f32_e32 v23, v56, v26
	v_add_f32_e32 v24, v57, v27
	v_cndmask_b32_e32 v2, v2, v13, vcc
	v_cndmask_b32_e64 v3, v3, 9, vcc
	v_cmp_gt_f32_e32 vcc, v15, v2
	s_waitcnt vmcnt(2) lgkmcnt(5)
	v_add_f32_e32 v25, v58, v28
	v_add_f32_e32 v26, v59, v29
	v_cndmask_b32_e32 v2, v2, v15, vcc
	v_cndmask_b32_e64 v3, v3, 10, vcc
	v_cmp_gt_f32_e32 vcc, v16, v2
	s_waitcnt lgkmcnt(4)
	v_add_f32_e32 v27, v60, v30
	v_add_f32_e32 v28, v61, v31
	v_cndmask_b32_e32 v2, v2, v16, vcc
	v_cndmask_b32_e64 v3, v3, 11, vcc
	v_cmp_gt_f32_e32 vcc, v17, v2
	s_waitcnt vmcnt(1) lgkmcnt(3)
	v_add_f32_e32 v29, v62, v34
	v_add_f32_e32 v30, v63, v35
	v_cndmask_b32_e32 v2, v2, v17, vcc
	v_cndmask_b32_e64 v3, v3, 12, vcc
	v_cmp_gt_f32_e32 vcc, v18, v2
	s_waitcnt lgkmcnt(2)
	v_add_f32_e32 v31, v64, v36
	v_add_f32_e32 v32, v65, v37
	v_cndmask_b32_e32 v2, v2, v18, vcc
	v_cndmask_b32_e64 v3, v3, 13, vcc
	v_cmp_gt_f32_e32 vcc, v19, v2
	s_waitcnt vmcnt(0) lgkmcnt(1)
	v_add_f32_e32 v33, v66, v38
	v_add_f32_e32 v34, v67, v39
	v_cndmask_b32_e32 v2, v2, v19, vcc
	v_cndmask_b32_e64 v3, v3, 14, vcc
	v_cmp_gt_f32_e32 vcc, v20, v2
	s_waitcnt lgkmcnt(0)
	v_add_f32_e32 v35, v68, v40
	v_add_f32_e32 v36, v69, v41
	v_cndmask_b32_e32 v2, v2, v20, vcc
	v_cndmask_b32_e64 v3, v3, 15, vcc
	v_cmp_gt_f32_e32 vcc, v21, v2
	s_nop 1
	v_cndmask_b32_e32 v2, v2, v21, vcc
	v_cndmask_b32_e64 v3, v3, 16, vcc
	v_cmp_gt_f32_e32 vcc, v22, v2
	s_nop 1
	v_cndmask_b32_e32 v2, v2, v22, vcc
	v_cndmask_b32_e64 v3, v3, 17, vcc
	v_cmp_gt_f32_e32 vcc, v23, v2
	s_nop 1
	v_cndmask_b32_e32 v2, v2, v23, vcc
	v_cndmask_b32_e64 v3, v3, 18, vcc
	v_cmp_gt_f32_e32 vcc, v24, v2
	s_nop 1
	v_cndmask_b32_e32 v2, v2, v24, vcc
	v_cndmask_b32_e64 v3, v3, 19, vcc
	v_cmp_gt_f32_e32 vcc, v25, v2
	s_nop 1
	v_cndmask_b32_e32 v2, v2, v25, vcc
	v_cndmask_b32_e64 v3, v3, 20, vcc
	v_cmp_gt_f32_e32 vcc, v26, v2
	s_nop 1
	v_cndmask_b32_e32 v2, v2, v26, vcc
	v_cndmask_b32_e64 v3, v3, 21, vcc
	v_cmp_gt_f32_e32 vcc, v27, v2
	s_nop 1
	v_cndmask_b32_e32 v2, v2, v27, vcc
	v_cndmask_b32_e64 v3, v3, 22, vcc
	v_cmp_gt_f32_e32 vcc, v28, v2
	s_nop 1
	v_cndmask_b32_e32 v2, v2, v28, vcc
	v_cndmask_b32_e64 v3, v3, 23, vcc
	v_cmp_gt_f32_e32 vcc, v29, v2
	s_nop 1
	v_cndmask_b32_e32 v2, v2, v29, vcc
	v_cndmask_b32_e64 v3, v3, 24, vcc
	v_cmp_gt_f32_e32 vcc, v30, v2
	s_nop 1
	v_cndmask_b32_e32 v2, v2, v30, vcc
	v_cndmask_b32_e64 v3, v3, 25, vcc
	v_cmp_gt_f32_e32 vcc, v31, v2
	s_nop 1
	v_cndmask_b32_e32 v2, v2, v31, vcc
	v_cndmask_b32_e64 v3, v3, 26, vcc
	v_cmp_gt_f32_e32 vcc, v32, v2
	s_nop 1
	v_cndmask_b32_e32 v2, v2, v32, vcc
	v_cndmask_b32_e64 v3, v3, 27, vcc
	v_cmp_gt_f32_e32 vcc, v33, v2
	s_nop 1
	v_cndmask_b32_e32 v2, v2, v33, vcc
	v_cndmask_b32_e64 v3, v3, 28, vcc
	v_cmp_gt_f32_e32 vcc, v34, v2
	s_nop 1
	v_cndmask_b32_e32 v2, v2, v34, vcc
	v_cndmask_b32_e64 v3, v3, 29, vcc
	v_cmp_gt_f32_e32 vcc, v35, v2
	s_nop 1
	v_cndmask_b32_e32 v37, v2, v35, vcc
	v_cndmask_b32_e64 v3, v3, 30, vcc
	v_cmp_gt_f32_e32 vcc, v36, v37
	s_nop 1
	v_cndmask_b32_e64 v2, v3, 31, vcc
	v_cndmask_b32_e32 v3, v37, v36, vcc
	v_mov_b32_e32 v37, 0xff800000
	v_cmp_ne_u32_e32 vcc, 0, v2
	s_nop 1
	v_cndmask_b32_e32 v38, v37, v1, vcc
	v_cmp_ne_u32_e32 vcc, 1, v2
	v_mov_b32_e32 v1, 1
	s_nop 0
	v_cndmask_b32_e32 v4, v37, v4, vcc
	v_cmp_ne_u32_e32 vcc, 2, v2
	s_nop 1
	v_cndmask_b32_e32 v39, v37, v6, vcc
	v_cmp_ne_u32_e32 vcc, 3, v2
	v_max_f32_e32 v6, 0xff800000, v38
	s_nop 0
	v_cndmask_b32_e32 v7, v37, v7, vcc
	v_cmp_ne_u32_e32 vcc, 4, v2
	s_nop 1
	v_cndmask_b32_e32 v8, v37, v8, vcc
	v_cmp_ne_u32_e32 vcc, 5, v2
	s_nop 1
	v_cndmask_b32_e32 v9, v37, v9, vcc
	v_cmp_ne_u32_e32 vcc, 6, v2
	s_nop 1
	v_cndmask_b32_e32 v10, v37, v10, vcc
	v_cmp_ne_u32_e32 vcc, 7, v2
	s_nop 1
	v_cndmask_b32_e32 v11, v37, v11, vcc
	v_cmp_ne_u32_e32 vcc, 8, v2
	s_nop 1
	v_cndmask_b32_e32 v12, v37, v12, vcc
	v_cmp_ne_u32_e32 vcc, 9, v2
	s_nop 1
	v_cndmask_b32_e32 v13, v37, v13, vcc
	v_cmp_ne_u32_e32 vcc, 10, v2
	s_nop 1
	v_cndmask_b32_e32 v15, v37, v15, vcc
	v_cmp_ne_u32_e32 vcc, 11, v2
	s_nop 1
	v_cndmask_b32_e32 v16, v37, v16, vcc
	v_cmp_ne_u32_e32 vcc, 12, v2
	s_nop 1
	v_cndmask_b32_e32 v17, v37, v17, vcc
	v_cmp_ne_u32_e32 vcc, 13, v2
	s_nop 1
	v_cndmask_b32_e32 v18, v37, v18, vcc
	v_cmp_ne_u32_e32 vcc, 14, v2
	s_nop 1
	v_cndmask_b32_e32 v19, v37, v19, vcc
	v_cmp_ne_u32_e32 vcc, 15, v2
	s_nop 1
	v_cndmask_b32_e32 v20, v37, v20, vcc
	v_cmp_ne_u32_e32 vcc, 16, v2
	s_nop 1
	v_cndmask_b32_e32 v21, v37, v21, vcc
	v_cmp_ne_u32_e32 vcc, 17, v2
	s_nop 1
	v_cndmask_b32_e32 v22, v37, v22, vcc
	v_cmp_ne_u32_e32 vcc, 18, v2
	s_nop 1
	v_cndmask_b32_e32 v23, v37, v23, vcc
	v_cmp_ne_u32_e32 vcc, 19, v2
	s_nop 1
	v_cndmask_b32_e32 v24, v37, v24, vcc
	v_cmp_ne_u32_e32 vcc, 20, v2
	s_nop 1
	v_cndmask_b32_e32 v25, v37, v25, vcc
	v_cmp_ne_u32_e32 vcc, 21, v2
	s_nop 1
	v_cndmask_b32_e32 v26, v37, v26, vcc
	v_cmp_ne_u32_e32 vcc, 22, v2
	s_nop 1
	v_cndmask_b32_e32 v27, v37, v27, vcc
	v_cmp_ne_u32_e32 vcc, 23, v2
	s_nop 1
	v_cndmask_b32_e32 v28, v37, v28, vcc
	v_cmp_ne_u32_e32 vcc, 24, v2
	s_nop 1
	v_cndmask_b32_e32 v29, v37, v29, vcc
	v_cmp_ne_u32_e32 vcc, 25, v2
	s_nop 1
	v_cndmask_b32_e32 v30, v37, v30, vcc
	v_cmp_ne_u32_e32 vcc, 26, v2
	s_nop 1
	v_cndmask_b32_e32 v31, v37, v31, vcc
	v_cmp_ne_u32_e32 vcc, 27, v2
	s_nop 1
	v_cndmask_b32_e32 v32, v37, v32, vcc
	v_cmp_ne_u32_e32 vcc, 28, v2
	s_nop 1
	v_cndmask_b32_e32 v33, v37, v33, vcc
	v_cmp_ne_u32_e32 vcc, 29, v2
	s_nop 1
	v_cndmask_b32_e32 v34, v37, v34, vcc
	v_cmp_ne_u32_e32 vcc, 30, v2
	s_nop 1
	v_cndmask_b32_e32 v35, v37, v35, vcc
	v_cmp_ne_u32_e32 vcc, 31, v2
	s_nop 1
	v_cndmask_b32_e32 v36, v37, v36, vcc
	v_cmp_gt_f32_e32 vcc, v4, v6
	s_nop 1
	v_cndmask_b32_e32 v6, v6, v4, vcc
	v_cndmask_b32_e64 v40, 0, 1, vcc
	v_cmp_gt_f32_e32 vcc, v39, v6
	s_nop 1
	v_cndmask_b32_e32 v6, v6, v39, vcc
	v_cndmask_b32_e64 v40, v40, 2, vcc
	v_cmp_gt_f32_e32 vcc, v7, v6
	s_nop 1
	v_cndmask_b32_e32 v6, v6, v7, vcc
	v_cndmask_b32_e64 v40, v40, 3, vcc
	v_cmp_gt_f32_e32 vcc, v8, v6
	s_nop 1
	v_cndmask_b32_e32 v6, v6, v8, vcc
	v_cndmask_b32_e64 v40, v40, 4, vcc
	v_cmp_gt_f32_e32 vcc, v9, v6
	s_nop 1
	v_cndmask_b32_e32 v6, v6, v9, vcc
	v_cndmask_b32_e64 v40, v40, 5, vcc
	v_cmp_gt_f32_e32 vcc, v10, v6
	s_nop 1
	v_cndmask_b32_e32 v6, v6, v10, vcc
	v_cndmask_b32_e64 v40, v40, 6, vcc
	v_cmp_gt_f32_e32 vcc, v11, v6
	s_nop 1
	v_cndmask_b32_e32 v6, v6, v11, vcc
	v_cndmask_b32_e64 v40, v40, 7, vcc
	v_cmp_gt_f32_e32 vcc, v12, v6
	s_nop 1
	v_cndmask_b32_e32 v6, v6, v12, vcc
	v_cndmask_b32_e64 v40, v40, 8, vcc
	v_cmp_gt_f32_e32 vcc, v13, v6
	s_nop 1
	v_cndmask_b32_e32 v6, v6, v13, vcc
	v_cndmask_b32_e64 v40, v40, 9, vcc
	v_cmp_gt_f32_e32 vcc, v15, v6
	s_nop 1
	v_cndmask_b32_e32 v6, v6, v15, vcc
	v_cndmask_b32_e64 v40, v40, 10, vcc
	v_cmp_gt_f32_e32 vcc, v16, v6
	s_nop 1
	v_cndmask_b32_e32 v6, v6, v16, vcc
	v_cndmask_b32_e64 v40, v40, 11, vcc
	v_cmp_gt_f32_e32 vcc, v17, v6
	s_nop 1
	v_cndmask_b32_e32 v6, v6, v17, vcc
	v_cndmask_b32_e64 v40, v40, 12, vcc
	v_cmp_gt_f32_e32 vcc, v18, v6
	s_nop 1
	v_cndmask_b32_e32 v6, v6, v18, vcc
	v_cndmask_b32_e64 v40, v40, 13, vcc
	v_cmp_gt_f32_e32 vcc, v19, v6
	s_nop 1
	v_cndmask_b32_e32 v6, v6, v19, vcc
	v_cndmask_b32_e64 v40, v40, 14, vcc
	v_cmp_gt_f32_e32 vcc, v20, v6
	s_nop 1
	v_cndmask_b32_e32 v6, v6, v20, vcc
	v_cndmask_b32_e64 v40, v40, 15, vcc
	v_cmp_gt_f32_e32 vcc, v21, v6
	s_nop 1
	v_cndmask_b32_e32 v6, v6, v21, vcc
	v_cndmask_b32_e64 v40, v40, 16, vcc
	v_cmp_gt_f32_e32 vcc, v22, v6
	s_nop 1
	v_cndmask_b32_e32 v6, v6, v22, vcc
	v_cndmask_b32_e64 v40, v40, 17, vcc
	v_cmp_gt_f32_e32 vcc, v23, v6
	s_nop 1
	v_cndmask_b32_e32 v6, v6, v23, vcc
	v_cndmask_b32_e64 v40, v40, 18, vcc
	v_cmp_gt_f32_e32 vcc, v24, v6
	s_nop 1
	v_cndmask_b32_e32 v6, v6, v24, vcc
	v_cndmask_b32_e64 v40, v40, 19, vcc
	v_cmp_gt_f32_e32 vcc, v25, v6
	s_nop 1
	v_cndmask_b32_e32 v6, v6, v25, vcc
	v_cndmask_b32_e64 v40, v40, 20, vcc
	v_cmp_gt_f32_e32 vcc, v26, v6
	s_nop 1
	v_cndmask_b32_e32 v6, v6, v26, vcc
	v_cndmask_b32_e64 v40, v40, 21, vcc
	v_cmp_gt_f32_e32 vcc, v27, v6
	s_nop 1
	v_cndmask_b32_e32 v6, v6, v27, vcc
	v_cndmask_b32_e64 v40, v40, 22, vcc
	v_cmp_gt_f32_e32 vcc, v28, v6
	s_nop 1
	v_cndmask_b32_e32 v6, v6, v28, vcc
	v_cndmask_b32_e64 v40, v40, 23, vcc
	v_cmp_gt_f32_e32 vcc, v29, v6
	s_nop 1
	v_cndmask_b32_e32 v6, v6, v29, vcc
	v_cndmask_b32_e64 v40, v40, 24, vcc
	v_cmp_gt_f32_e32 vcc, v30, v6
	s_nop 1
	v_cndmask_b32_e32 v6, v6, v30, vcc
	v_cndmask_b32_e64 v40, v40, 25, vcc
	v_cmp_gt_f32_e32 vcc, v31, v6
	s_nop 1
	v_cndmask_b32_e32 v6, v6, v31, vcc
	v_cndmask_b32_e64 v40, v40, 26, vcc
	v_cmp_gt_f32_e32 vcc, v32, v6
	s_nop 1
	v_cndmask_b32_e32 v6, v6, v32, vcc
	v_cndmask_b32_e64 v40, v40, 27, vcc
	v_cmp_gt_f32_e32 vcc, v33, v6
	s_nop 1
	v_cndmask_b32_e32 v6, v6, v33, vcc
	v_cndmask_b32_e64 v40, v40, 28, vcc
	v_cmp_gt_f32_e32 vcc, v34, v6
	s_nop 1
	v_cndmask_b32_e32 v6, v6, v34, vcc
	v_cndmask_b32_e64 v40, v40, 29, vcc
	v_cmp_gt_f32_e32 vcc, v35, v6
	s_nop 1
	v_cndmask_b32_e32 v41, v6, v35, vcc
	v_cndmask_b32_e64 v40, v40, 30, vcc
	v_cmp_gt_f32_e32 vcc, v36, v41
	s_nop 1
	v_cndmask_b32_e64 v6, v40, 31, vcc
	v_cndmask_b32_e32 v40, v41, v36, vcc
	v_cmp_ne_u32_e32 vcc, 0, v6
	s_nop 1
	v_cndmask_b32_e32 v38, v37, v38, vcc
	v_cmp_ne_u32_e32 vcc, 1, v6
	s_nop 1
	v_cndmask_b32_e32 v4, v37, v4, vcc
	v_cmp_ne_u32_e32 vcc, 2, v6
	s_nop 1
	v_cndmask_b32_e32 v39, v37, v39, vcc
	v_cmp_ne_u32_e32 vcc, 3, v6
	s_nop 1
	v_cndmask_b32_e32 v7, v37, v7, vcc
	v_cmp_ne_u32_e32 vcc, 4, v6
	s_nop 1
	v_cndmask_b32_e32 v8, v37, v8, vcc
	v_cmp_ne_u32_e32 vcc, 5, v6
	s_nop 1
	v_cndmask_b32_e32 v9, v37, v9, vcc
	v_cmp_ne_u32_e32 vcc, 6, v6
	s_nop 1
	v_cndmask_b32_e32 v41, v37, v10, vcc
	v_cmp_ne_u32_e32 vcc, 7, v6
	v_max_f32_e32 v10, 0xff800000, v38
	s_nop 0
	v_cndmask_b32_e32 v11, v37, v11, vcc
	v_cmp_ne_u32_e32 vcc, 8, v6
	s_nop 1
	v_cndmask_b32_e32 v12, v37, v12, vcc
	v_cmp_ne_u32_e32 vcc, 9, v6
	s_nop 1
	v_cndmask_b32_e32 v13, v37, v13, vcc
	v_cmp_ne_u32_e32 vcc, 10, v6
	s_nop 1
	v_cndmask_b32_e32 v15, v37, v15, vcc
	v_cmp_ne_u32_e32 vcc, 11, v6
	s_nop 1
	v_cndmask_b32_e32 v16, v37, v16, vcc
	v_cmp_ne_u32_e32 vcc, 12, v6
	s_nop 1
	v_cndmask_b32_e32 v17, v37, v17, vcc
	v_cmp_ne_u32_e32 vcc, 13, v6
	s_nop 1
	v_cndmask_b32_e32 v18, v37, v18, vcc
	v_cmp_ne_u32_e32 vcc, 14, v6
	s_nop 1
	v_cndmask_b32_e32 v19, v37, v19, vcc
	v_cmp_ne_u32_e32 vcc, 15, v6
	s_nop 1
	v_cndmask_b32_e32 v20, v37, v20, vcc
	v_cmp_ne_u32_e32 vcc, 16, v6
	s_nop 1
	v_cndmask_b32_e32 v21, v37, v21, vcc
	v_cmp_ne_u32_e32 vcc, 17, v6
	s_nop 1
	v_cndmask_b32_e32 v22, v37, v22, vcc
	v_cmp_ne_u32_e32 vcc, 18, v6
	s_nop 1
	v_cndmask_b32_e32 v23, v37, v23, vcc
	v_cmp_ne_u32_e32 vcc, 19, v6
	s_nop 1
	v_cndmask_b32_e32 v24, v37, v24, vcc
	v_cmp_ne_u32_e32 vcc, 20, v6
	s_nop 1
	v_cndmask_b32_e32 v25, v37, v25, vcc
	v_cmp_ne_u32_e32 vcc, 21, v6
	s_nop 1
	v_cndmask_b32_e32 v26, v37, v26, vcc
	v_cmp_ne_u32_e32 vcc, 22, v6
	s_nop 1
	v_cndmask_b32_e32 v27, v37, v27, vcc
	v_cmp_ne_u32_e32 vcc, 23, v6
	s_nop 1
	v_cndmask_b32_e32 v28, v37, v28, vcc
	v_cmp_ne_u32_e32 vcc, 24, v6
	s_nop 1
	v_cndmask_b32_e32 v29, v37, v29, vcc
	v_cmp_ne_u32_e32 vcc, 25, v6
	s_nop 1
	v_cndmask_b32_e32 v30, v37, v30, vcc
	v_cmp_ne_u32_e32 vcc, 26, v6
	s_nop 1
	v_cndmask_b32_e32 v31, v37, v31, vcc
	v_cmp_ne_u32_e32 vcc, 27, v6
	s_nop 1
	v_cndmask_b32_e32 v32, v37, v32, vcc
	v_cmp_ne_u32_e32 vcc, 28, v6
	s_nop 1
	v_cndmask_b32_e32 v33, v37, v33, vcc
	v_cmp_ne_u32_e32 vcc, 29, v6
	s_nop 1
	v_cndmask_b32_e32 v34, v37, v34, vcc
	v_cmp_ne_u32_e32 vcc, 30, v6
	s_nop 1
	v_cndmask_b32_e32 v35, v37, v35, vcc
	v_cmp_ne_u32_e32 vcc, 31, v6
	s_nop 1
	v_cndmask_b32_e32 v36, v37, v36, vcc
	v_cmp_gt_f32_e32 vcc, v4, v10
	s_nop 1
	v_cndmask_b32_e32 v10, v10, v4, vcc
	v_cndmask_b32_e64 v42, 0, 1, vcc
	v_cmp_gt_f32_e32 vcc, v39, v10
	s_nop 1
	v_cndmask_b32_e32 v10, v10, v39, vcc
	v_cndmask_b32_e64 v42, v42, 2, vcc
	v_cmp_gt_f32_e32 vcc, v7, v10
	s_nop 1
	v_cndmask_b32_e32 v10, v10, v7, vcc
	v_cndmask_b32_e64 v42, v42, 3, vcc
	v_cmp_gt_f32_e32 vcc, v8, v10
	s_nop 1
	v_cndmask_b32_e32 v10, v10, v8, vcc
	v_cndmask_b32_e64 v42, v42, 4, vcc
	v_cmp_gt_f32_e32 vcc, v9, v10
	s_nop 1
	v_cndmask_b32_e32 v10, v10, v9, vcc
	v_cndmask_b32_e64 v42, v42, 5, vcc
	v_cmp_gt_f32_e32 vcc, v41, v10
	s_nop 1
	v_cndmask_b32_e32 v10, v10, v41, vcc
	v_cndmask_b32_e64 v42, v42, 6, vcc
	v_cmp_gt_f32_e32 vcc, v11, v10
	s_nop 1
	v_cndmask_b32_e32 v10, v10, v11, vcc
	v_cndmask_b32_e64 v42, v42, 7, vcc
	v_cmp_gt_f32_e32 vcc, v12, v10
	s_nop 1
	v_cndmask_b32_e32 v10, v10, v12, vcc
	v_cndmask_b32_e64 v42, v42, 8, vcc
	v_cmp_gt_f32_e32 vcc, v13, v10
	s_nop 1
	v_cndmask_b32_e32 v10, v10, v13, vcc
	v_cndmask_b32_e64 v42, v42, 9, vcc
	v_cmp_gt_f32_e32 vcc, v15, v10
	s_nop 1
	v_cndmask_b32_e32 v10, v10, v15, vcc
	v_cndmask_b32_e64 v42, v42, 10, vcc
	v_cmp_gt_f32_e32 vcc, v16, v10
	s_nop 1
	v_cndmask_b32_e32 v10, v10, v16, vcc
	v_cndmask_b32_e64 v42, v42, 11, vcc
	v_cmp_gt_f32_e32 vcc, v17, v10
	s_nop 1
	v_cndmask_b32_e32 v10, v10, v17, vcc
	v_cndmask_b32_e64 v42, v42, 12, vcc
	v_cmp_gt_f32_e32 vcc, v18, v10
	s_nop 1
	v_cndmask_b32_e32 v10, v10, v18, vcc
	v_cndmask_b32_e64 v42, v42, 13, vcc
	v_cmp_gt_f32_e32 vcc, v19, v10
	s_nop 1
	v_cndmask_b32_e32 v10, v10, v19, vcc
	v_cndmask_b32_e64 v42, v42, 14, vcc
	v_cmp_gt_f32_e32 vcc, v20, v10
	s_nop 1
	v_cndmask_b32_e32 v10, v10, v20, vcc
	v_cndmask_b32_e64 v42, v42, 15, vcc
	v_cmp_gt_f32_e32 vcc, v21, v10
	s_nop 1
	v_cndmask_b32_e32 v10, v10, v21, vcc
	v_cndmask_b32_e64 v42, v42, 16, vcc
	v_cmp_gt_f32_e32 vcc, v22, v10
	s_nop 1
	v_cndmask_b32_e32 v10, v10, v22, vcc
	v_cndmask_b32_e64 v42, v42, 17, vcc
	v_cmp_gt_f32_e32 vcc, v23, v10
	s_nop 1
	v_cndmask_b32_e32 v10, v10, v23, vcc
	v_cndmask_b32_e64 v42, v42, 18, vcc
	v_cmp_gt_f32_e32 vcc, v24, v10
	s_nop 1
	v_cndmask_b32_e32 v10, v10, v24, vcc
	v_cndmask_b32_e64 v42, v42, 19, vcc
	v_cmp_gt_f32_e32 vcc, v25, v10
	s_nop 1
	v_cndmask_b32_e32 v10, v10, v25, vcc
	v_cndmask_b32_e64 v42, v42, 20, vcc
	v_cmp_gt_f32_e32 vcc, v26, v10
	s_nop 1
	v_cndmask_b32_e32 v10, v10, v26, vcc
	v_cndmask_b32_e64 v42, v42, 21, vcc
	v_cmp_gt_f32_e32 vcc, v27, v10
	s_nop 1
	v_cndmask_b32_e32 v10, v10, v27, vcc
	v_cndmask_b32_e64 v42, v42, 22, vcc
	v_cmp_gt_f32_e32 vcc, v28, v10
	s_nop 1
	v_cndmask_b32_e32 v10, v10, v28, vcc
	v_cndmask_b32_e64 v42, v42, 23, vcc
	v_cmp_gt_f32_e32 vcc, v29, v10
	s_nop 1
	v_cndmask_b32_e32 v10, v10, v29, vcc
	v_cndmask_b32_e64 v42, v42, 24, vcc
	v_cmp_gt_f32_e32 vcc, v30, v10
	s_nop 1
	v_cndmask_b32_e32 v10, v10, v30, vcc
	v_cndmask_b32_e64 v42, v42, 25, vcc
	v_cmp_gt_f32_e32 vcc, v31, v10
	s_nop 1
	v_cndmask_b32_e32 v10, v10, v31, vcc
	v_cndmask_b32_e64 v42, v42, 26, vcc
	v_cmp_gt_f32_e32 vcc, v32, v10
	s_nop 1
	v_cndmask_b32_e32 v10, v10, v32, vcc
	v_cndmask_b32_e64 v42, v42, 27, vcc
	v_cmp_gt_f32_e32 vcc, v33, v10
	s_nop 1
	v_cndmask_b32_e32 v10, v10, v33, vcc
	v_cndmask_b32_e64 v42, v42, 28, vcc
	v_cmp_gt_f32_e32 vcc, v34, v10
	s_nop 1
	v_cndmask_b32_e32 v10, v10, v34, vcc
	v_cndmask_b32_e64 v42, v42, 29, vcc
	v_cmp_gt_f32_e32 vcc, v35, v10
	s_nop 1
	v_cndmask_b32_e32 v43, v10, v35, vcc
	v_cndmask_b32_e64 v42, v42, 30, vcc
	v_cmp_gt_f32_e32 vcc, v36, v43
	s_nop 1
	v_cndmask_b32_e64 v10, v42, 31, vcc
	v_cndmask_b32_e32 v42, v43, v36, vcc
	v_cmp_ne_u32_e32 vcc, 0, v10
	s_nop 1
	v_cndmask_b32_e32 v38, v37, v38, vcc
	v_cmp_ne_u32_e32 vcc, 1, v10
	s_nop 1
	v_cndmask_b32_e32 v4, v37, v4, vcc
	v_cmp_ne_u32_e32 vcc, 2, v10
	s_nop 1
	v_cndmask_b32_e32 v39, v37, v39, vcc
	v_cmp_ne_u32_e32 vcc, 3, v10
	s_nop 1
	v_cndmask_b32_e32 v7, v37, v7, vcc
	v_cmp_ne_u32_e32 vcc, 4, v10
	s_nop 1
	v_cndmask_b32_e32 v8, v37, v8, vcc
	v_cmp_ne_u32_e32 vcc, 5, v10
	s_nop 1
	v_cndmask_b32_e32 v9, v37, v9, vcc
	v_cmp_ne_u32_e32 vcc, 6, v10
	s_nop 1
	v_cndmask_b32_e32 v41, v37, v41, vcc
	v_cmp_ne_u32_e32 vcc, 7, v10
	s_nop 1
	v_cndmask_b32_e32 v11, v37, v11, vcc
	v_cmp_ne_u32_e32 vcc, 8, v10
	s_nop 1
	v_cndmask_b32_e32 v12, v37, v12, vcc
	v_cmp_ne_u32_e32 vcc, 9, v10
	s_nop 1
	v_cndmask_b32_e32 v13, v37, v13, vcc
	v_cmp_ne_u32_e32 vcc, 10, v10
	s_nop 1
	v_cndmask_b32_e32 v15, v37, v15, vcc
	v_cmp_ne_u32_e32 vcc, 11, v10
	s_nop 1
	v_cndmask_b32_e32 v16, v37, v16, vcc
	v_cmp_ne_u32_e32 vcc, 12, v10
	s_nop 1
	v_cndmask_b32_e32 v17, v37, v17, vcc
	v_cmp_ne_u32_e32 vcc, 13, v10
	s_nop 1
	v_cndmask_b32_e32 v18, v37, v18, vcc
	v_cmp_ne_u32_e32 vcc, 14, v10
	s_nop 1
	v_cndmask_b32_e32 v19, v37, v19, vcc
	v_cmp_ne_u32_e32 vcc, 15, v10
	s_nop 1
	v_cndmask_b32_e32 v20, v37, v20, vcc
	v_cmp_ne_u32_e32 vcc, 16, v10
	s_nop 1
	v_cndmask_b32_e32 v21, v37, v21, vcc
	v_cmp_ne_u32_e32 vcc, 17, v10
	s_nop 1
	v_cndmask_b32_e32 v22, v37, v22, vcc
	v_cmp_ne_u32_e32 vcc, 18, v10
	s_nop 1
	v_cndmask_b32_e32 v23, v37, v23, vcc
	v_cmp_ne_u32_e32 vcc, 19, v10
	s_nop 1
	v_cndmask_b32_e32 v24, v37, v24, vcc
	v_cmp_ne_u32_e32 vcc, 20, v10
	s_nop 1
	v_cndmask_b32_e32 v25, v37, v25, vcc
	v_cmp_ne_u32_e32 vcc, 21, v10
	s_nop 1
	v_cndmask_b32_e32 v26, v37, v26, vcc
	v_cmp_ne_u32_e32 vcc, 22, v10
	s_nop 1
	v_cndmask_b32_e32 v27, v37, v27, vcc
	v_cmp_ne_u32_e32 vcc, 23, v10
	s_nop 1
	v_cndmask_b32_e32 v28, v37, v28, vcc
	v_cmp_ne_u32_e32 vcc, 24, v10
	s_nop 1
	v_cndmask_b32_e32 v29, v37, v29, vcc
	v_cmp_ne_u32_e32 vcc, 25, v10
	s_nop 1
	v_cndmask_b32_e32 v30, v37, v30, vcc
	v_cmp_ne_u32_e32 vcc, 26, v10
	s_nop 1
	v_cndmask_b32_e32 v31, v37, v31, vcc
	v_cmp_ne_u32_e32 vcc, 27, v10
	s_nop 1
	v_cndmask_b32_e32 v32, v37, v32, vcc
	v_cmp_ne_u32_e32 vcc, 28, v10
	s_nop 1
	v_cndmask_b32_e32 v33, v37, v33, vcc
	v_cmp_ne_u32_e32 vcc, 29, v10
	s_nop 1
	v_cndmask_b32_e32 v34, v37, v34, vcc
	v_cmp_ne_u32_e32 vcc, 30, v10
	s_nop 1
	v_cndmask_b32_e32 v35, v37, v35, vcc
	v_cmp_ne_u32_e32 vcc, 31, v10
	s_nop 1
	v_cndmask_b32_e32 v36, v37, v36, vcc
	v_max_f32_e32 v37, 0xff800000, v38
	v_cmp_gt_f32_e32 vcc, v4, v37
	s_nop 1
	v_cndmask_b32_e32 v4, v37, v4, vcc
	v_cndmask_b32_e64 v38, 0, 1, vcc
	v_cmp_gt_f32_e32 vcc, v39, v4
	s_nop 1
	v_cndmask_b32_e32 v4, v4, v39, vcc
	v_cndmask_b32_e64 v37, v38, 2, vcc
	v_cmp_gt_f32_e32 vcc, v7, v4
	s_nop 1
	v_cndmask_b32_e32 v4, v4, v7, vcc
	v_cndmask_b32_e64 v37, v37, 3, vcc
	v_cmp_gt_f32_e32 vcc, v8, v4
	s_nop 1
	v_cndmask_b32_e32 v4, v4, v8, vcc
	v_cndmask_b32_e64 v7, v37, 4, vcc
	v_cmp_gt_f32_e32 vcc, v9, v4
	s_nop 1
	v_cndmask_b32_e32 v4, v4, v9, vcc
	v_cndmask_b32_e64 v7, v7, 5, vcc
	v_cmp_gt_f32_e32 vcc, v41, v4
	s_nop 1
	v_cndmask_b32_e32 v4, v4, v41, vcc
	v_cndmask_b32_e64 v7, v7, 6, vcc
	v_cmp_gt_f32_e32 vcc, v11, v4
	s_nop 1
	v_cndmask_b32_e32 v4, v4, v11, vcc
	v_cndmask_b32_e64 v7, v7, 7, vcc
	v_cmp_gt_f32_e32 vcc, v12, v4
	s_nop 1
	v_cndmask_b32_e32 v4, v4, v12, vcc
	v_cndmask_b32_e64 v7, v7, 8, vcc
	v_cmp_gt_f32_e32 vcc, v13, v4
	s_nop 1
	v_cndmask_b32_e32 v4, v4, v13, vcc
	v_cndmask_b32_e64 v7, v7, 9, vcc
	v_cmp_gt_f32_e32 vcc, v15, v4
	s_nop 1
	v_cndmask_b32_e32 v4, v4, v15, vcc
	v_cndmask_b32_e64 v7, v7, 10, vcc
	v_cmp_gt_f32_e32 vcc, v16, v4
	v_ashrrev_i32_e32 v15, 31, v14
	v_lshlrev_b64 v[12:13], 6, v[14:15]
	v_cndmask_b32_e32 v4, v4, v16, vcc
	v_cndmask_b32_e64 v7, v7, 11, vcc
	v_cmp_gt_f32_e32 vcc, v17, v4
	v_lshl_add_u64 v[12:13], s[6:7], 0, v[12:13]
	s_nop 0
	v_cndmask_b32_e32 v4, v4, v17, vcc
	v_cndmask_b32_e64 v7, v7, 12, vcc
	v_cmp_gt_f32_e32 vcc, v18, v4
	s_nop 1
	v_cndmask_b32_e32 v4, v4, v18, vcc
	v_cndmask_b32_e64 v7, v7, 13, vcc
	v_cmp_gt_f32_e32 vcc, v19, v4
	s_nop 1
	v_cndmask_b32_e32 v4, v4, v19, vcc
	v_cndmask_b32_e64 v7, v7, 14, vcc
	v_cmp_gt_f32_e32 vcc, v20, v4
	s_nop 1
	v_cndmask_b32_e32 v4, v4, v20, vcc
	v_cndmask_b32_e64 v7, v7, 15, vcc
	v_cmp_gt_f32_e32 vcc, v21, v4
	s_nop 1
	v_cndmask_b32_e32 v11, v4, v21, vcc
	v_lshlrev_b32_e32 v4, 5, v2
	v_lshl_add_u64 v[8:9], v[4:5], 2, s[10:11]
	v_lshl_add_u32 v70, v2, 2, v72
	ds_add_rtn_u32 v8, v70, v73
	v_cndmask_b32_e64 v7, v7, 16, vcc
	v_cmp_gt_f32_e32 vcc, v22, v11
	v_sub_f32_e32 v9, v40, v3
	v_mul_f32_e32 v9, 0x3fb8aa3b, v9
	v_cndmask_b32_e64 v4, v7, 17, vcc
	v_cndmask_b32_e32 v7, v11, v22, vcc
	v_cmp_gt_f32_e32 vcc, v23, v7
	v_exp_f32_e32 v11, v9
	v_sub_f32_e32 v9, v42, v3
	v_cndmask_b32_e32 v7, v7, v23, vcc
	v_cndmask_b32_e64 v4, v4, 18, vcc
	v_cmp_gt_f32_e32 vcc, v24, v7
	v_mul_f32_e32 v9, 0x3fb8aa3b, v9
	v_exp_f32_e32 v17, v9
	v_cndmask_b32_e32 v7, v7, v24, vcc
	v_cndmask_b32_e64 v4, v4, 19, vcc
	v_cmp_gt_f32_e32 vcc, v25, v7
	s_nop 1
	v_cndmask_b32_e32 v7, v7, v25, vcc
	v_cndmask_b32_e64 v4, v4, 20, vcc
	v_cmp_gt_f32_e32 vcc, v26, v7
	s_nop 1
	v_cndmask_b32_e32 v7, v7, v26, vcc
	v_cndmask_b32_e64 v4, v4, 21, vcc
	v_cmp_gt_f32_e32 vcc, v27, v7
	s_nop 1
	v_cndmask_b32_e32 v7, v7, v27, vcc
	v_cndmask_b32_e64 v4, v4, 22, vcc
	v_cmp_gt_f32_e32 vcc, v28, v7
	s_nop 1
	v_cndmask_b32_e32 v7, v7, v28, vcc
	v_cndmask_b32_e64 v4, v4, 23, vcc
	v_cmp_gt_f32_e32 vcc, v29, v7
	s_nop 1
	v_cndmask_b32_e32 v7, v7, v29, vcc
	v_cndmask_b32_e64 v4, v4, 24, vcc
	v_cmp_gt_f32_e32 vcc, v30, v7
	s_nop 1
	v_cndmask_b32_e32 v7, v7, v30, vcc
	v_cndmask_b32_e64 v4, v4, 25, vcc
	v_cmp_gt_f32_e32 vcc, v31, v7
	s_nop 1
	v_cndmask_b32_e32 v7, v7, v31, vcc
	v_cndmask_b32_e64 v4, v4, 26, vcc
	v_cmp_gt_f32_e32 vcc, v32, v7
	s_nop 1
	v_cndmask_b32_e32 v7, v7, v32, vcc
	v_cndmask_b32_e64 v4, v4, 27, vcc
	v_cmp_gt_f32_e32 vcc, v33, v7
	s_nop 1
	v_cndmask_b32_e32 v7, v7, v33, vcc
	v_cndmask_b32_e64 v4, v4, 28, vcc
	v_cmp_gt_f32_e32 vcc, v34, v7
	s_nop 1
	v_cndmask_b32_e32 v7, v7, v34, vcc
	v_cndmask_b32_e64 v4, v4, 29, vcc
	v_cmp_gt_f32_e32 vcc, v35, v7
	s_nop 1
	v_cndmask_b32_e32 v7, v7, v35, vcc
	v_cndmask_b32_e64 v4, v4, 30, vcc
	v_cmp_gt_f32_e32 vcc, v36, v7
	s_nop 1
	v_cndmask_b32_e64 v16, v4, 31, vcc
	v_lshl_add_u32 v70, v6, 2, v72
	ds_add_rtn_u32 v74, v70, v73
	v_lshl_add_u32 v70, v10, 2, v72
	ds_add_rtn_u32 v75, v70, v73
	v_lshl_add_u32 v70, v16, 2, v72
	ds_add_rtn_u32 v76, v70, v73
	v_cndmask_b32_e32 v4, v7, v36, vcc
	v_sub_f32_e32 v7, v3, v3
	v_mul_f32_e32 v7, 0x3fb8aa3b, v7
	v_exp_f32_e32 v7, v7
	v_sub_f32_e32 v3, v4, v3
	v_mul_f32_e32 v3, 0x3fb8aa3b, v3
	v_exp_f32_e32 v22, v3
	v_add_f32_e32 v3, 0, v7
	v_add_f32_e32 v3, v3, v11
	v_add_f32_e32 v3, v3, v17
	v_add_f32_e32 v3, v3, v22
	v_div_scale_f32 v4, s[2:3], v3, v3, 1.0
	v_rcp_f32_e32 v9, v4
	s_mov_b32 s2, 0x5e30000
	v_fma_f32 v15, -v4, v9, 1.0
	v_fmac_f32_e32 v9, v15, v9
	v_div_scale_f32 v15, vcc, 1.0, v3, 1.0
	v_mul_f32_e32 v18, v15, v9
	v_fma_f32 v19, -v4, v18, v15
	v_fmac_f32_e32 v18, v19, v9
	v_fma_f32 v4, -v4, v18, v15
	v_div_fmas_f32 v4, v4, v9, v18
	v_div_fixup_f32 v15, v4, v3, 1.0
	v_mov_b32_e32 v3, v5
	v_lshlrev_b64 v[18:19], 16, v[2:3]
.LBB0_1279:
	s_or_b64 exec, exec, s[4:5]
	s_waitcnt lgkmcnt(0)
	s_barrier
	v_readfirstlane_b32 s100, v0
	s_nop 0
	s_cmp_lt_u32 s100, 64
	s_cbranch_scc0 .Lp8_noagg
	v_mbcnt_lo_u32_b32 v77, -1, 0
	v_mbcnt_hi_u32_b32 v77, -1, v77
	v_cmp_gt_u32_e32 vcc, 32, v77
	s_and_saveexec_b64 s[100:101], vcc
	v_lshlrev_b32_e32 v78, 2, v77
	v_add_u32_e32 v78, 0x21040, v78
	ds_read_b32 v79, v78
	v_lshlrev_b32_e32 v80, 7, v77
	s_add_u32 s10, s6, 0x4600
	s_addc_u32 s11, s7, 0
	s_waitcnt lgkmcnt(0)
	global_atomic_add v81, v80, v79, s[10:11] sc0
	s_waitcnt vmcnt(0)
	ds_write_b32 v78, v81 offset:256
	s_waitcnt lgkmcnt(0)
	s_or_b64 exec, exec, s[100:101]
.Lp8_noagg:
	s_barrier
	s_and_saveexec_b64 s[4:5], s[96:97]
	s_cbranch_execz .Lp8_p2done
	v_lshl_add_u32 v70, v2, 2, v72
	ds_read_b32 v77, v70 offset:256
	v_lshl_add_u32 v70, v6, 2, v72
	ds_read_b32 v78, v70 offset:256
	v_lshl_add_u32 v70, v10, 2, v72
	ds_read_b32 v79, v70 offset:256
	v_lshl_add_u32 v70, v16, 2, v72
	ds_read_b32 v80, v70 offset:256
	s_waitcnt lgkmcnt(0)
	v_add_u32_e32 v8, v8, v77
	v_add_u32_e32 v74, v74, v78
	v_add_u32_e32 v75, v75, v79
	v_add_u32_e32 v76, v76, v80
	v_ashrrev_i32_e32 v9, 31, v8
	v_lshl_add_u64 v[18:19], s[8:9], 0, v[18:19]
	v_lshl_add_u64 v[18:19], v[8:9], 2, v[18:19]
	v_mov_b32_e32 v3, v8
	v_add_co_u32_e32 v8, vcc, s2, v12
	v_mul_f32_e32 v4, v7, v15
	s_nop 0
	v_addc_co_u32_e32 v9, vcc, 0, v13, vcc
	global_store_dword v[18:19], v14, off
	global_store_dwordx4 v[8:9], v[2:5], off
	v_mov_b32_e32 v7, v5
	v_lshlrev_b64 v[8:9], 16, v[6:7]
	v_mov_b32_e32 v2, v74
	v_lshl_add_u64 v[8:9], s[8:9], 0, v[8:9]
	s_mov_b64 s[2:3], 0x5e30000
	v_lshl_add_u64 v[20:21], v[12:13], 0, s[2:3]
	v_lshlrev_b32_e32 v4, 5, v10
	v_mul_f32_e32 v12, v17, v15
	v_mov_b32_e32 v13, v5
	v_mov_b32_e32 v17, v5
	v_mul_f32_e32 v18, v22, v15
	v_mov_b32_e32 v19, v5
	v_ashrrev_i32_e32 v3, 31, v2
	v_lshl_add_u64 v[8:9], v[2:3], 2, v[8:9]
	global_store_dword v[8:9], v14, off
	v_mul_f32_e32 v8, v11, v15
	v_mov_b32_e32 v7, v2
	v_mov_b32_e32 v9, v5
	global_store_dwordx4 v[20:21], v[6:9], off offset:16
	v_mov_b32_e32 v2, v75
	v_mov_b32_e32 v11, v5
	v_lshlrev_b64 v[6:7], 16, v[10:11]
	v_lshl_add_u64 v[6:7], s[8:9], 0, v[6:7]
	v_lshlrev_b32_e32 v4, 5, v16
	v_ashrrev_i32_e32 v3, 31, v2
	v_lshl_add_u64 v[6:7], v[2:3], 2, v[6:7]
	v_mov_b32_e32 v11, v2
	global_store_dword v[6:7], v14, off
	global_store_dwordx4 v[20:21], v[10:13], off offset:32
	v_mov_b32_e32 v2, v76
	v_lshlrev_b64 v[6:7], 16, v[16:17]
	v_lshl_add_u64 v[6:7], s[8:9], 0, v[6:7]
	v_ashrrev_i32_e32 v3, 31, v2
	v_lshl_add_u64 v[6:7], v[2:3], 2, v[6:7]
	v_mov_b32_e32 v17, v2
	global_store_dword v[6:7], v14, off
	global_store_dwordx4 v[20:21], v[16:19], off offset:48
